# P2 slab stores and P3 Y stores also sc0 sc1 (same policy as the P4 output stores)
# speedup vs baseline: 1.0066x; 1.0066x over previous
.Lp2_at_skip:
	s_lshl_b32 s1, s30, 22
	s_mov_b32 s0, 0x3d800000
	s_nop 15
	s_nop 15
	v_pk_mul_f32 v[8:9], v[190:191], s[0:1] op_sel_hi:[1,0]
	v_pk_mul_f32 v[16:17], v[186:187], s[0:1] op_sel_hi:[1,0]
	v_pk_mul_f32 v[20:21], v[182:183], s[0:1] op_sel_hi:[1,0]
	v_pk_mul_f32 v[24:25], v[178:179], s[0:1] op_sel_hi:[1,0]
	v_cvt_pk_fp8_f32 v6, v8, v9
	v_lshlrev_b32_e32 v1, 4, v202
	v_cvt_pk_fp8_f32 v7, v16, v17
	v_cvt_pk_fp8_f32 v8, v20, v21
	v_cvt_pk_fp8_f32 v9, v24, v25
	v_lshl_or_b32 v1, s39, 6, v1
	v_or_b32_e32 v2, s24, v1
	v_lshl_or_b32 v1, s29, 8, v197
	v_pk_mul_f32 v[12:13], v[192:193], s[0:1] op_sel_hi:[1,0]
	v_pk_mul_f32 v[14:15], v[188:189], s[0:1] op_sel_hi:[1,0]
	v_pk_mul_f32 v[18:19], v[184:185], s[0:1] op_sel_hi:[1,0]
	v_pk_mul_f32 v[22:23], v[180:181], s[0:1] op_sel_hi:[1,0]
	v_lshl_add_u32 v4, s28, 6, v1
	v_mov_b32_e32 v5, 0
	v_cvt_pk_fp8_f32 v6, v12, v13 op_sel:[0,0,1]
	v_cvt_pk_fp8_f32 v7, v14, v15 op_sel:[0,0,1]
	v_cvt_pk_fp8_f32 v8, v18, v19 op_sel:[0,0,1]
	v_cvt_pk_fp8_f32 v9, v22, v23 op_sel:[0,0,1]
	s_add_u32 s6, s6, s1
	v_lshlrev_b64 v[10:11], 11, v[4:5]
	s_addc_u32 s7, s7, 0
	v_ashrrev_i32_e32 v3, 31, v2
	v_lshl_add_u64 v[10:11], s[6:7], 0, v[10:11]
	v_lshl_add_u64 v[10:11], v[10:11], 0, v[2:3]
	global_store_dwordx4 v[10:11], v[6:9], off sc0 sc1
	v_pk_mul_f32 v[16:17], v[170:171], s[0:1] op_sel_hi:[1,0]
	v_pk_mul_f32 v[20:21], v[166:167], s[0:1] op_sel_hi:[1,0]
	v_pk_mul_f32 v[8:9], v[174:175], s[0:1] op_sel_hi:[1,0]
	v_pk_mul_f32 v[24:25], v[162:163], s[0:1] op_sel_hi:[1,0]
	v_cvt_pk_fp8_f32 v6, v8, v9
	v_pk_mul_f32 v[12:13], v[176:177], s[0:1] op_sel_hi:[1,0]
	v_cvt_pk_fp8_f32 v7, v16, v17
	v_cvt_pk_fp8_f32 v8, v20, v21
	v_cvt_pk_fp8_f32 v9, v24, v25
	v_pk_mul_f32 v[14:15], v[172:173], s[0:1] op_sel_hi:[1,0]
	v_pk_mul_f32 v[18:19], v[168:169], s[0:1] op_sel_hi:[1,0]
	v_pk_mul_f32 v[22:23], v[164:165], s[0:1] op_sel_hi:[1,0]
	v_or_b32_e32 v10, 16, v4
	v_mov_b32_e32 v11, v5
	v_cvt_pk_fp8_f32 v6, v12, v13 op_sel:[0,0,1]
	v_cvt_pk_fp8_f32 v7, v14, v15 op_sel:[0,0,1]
	v_cvt_pk_fp8_f32 v8, v18, v19 op_sel:[0,0,1]
	v_cvt_pk_fp8_f32 v9, v22, v23 op_sel:[0,0,1]
	v_lshlrev_b64 v[10:11], 11, v[10:11]
	v_lshl_add_u64 v[10:11], s[6:7], 0, v[10:11]
	v_lshl_add_u64 v[10:11], v[10:11], 0, v[2:3]
	global_store_dwordx4 v[10:11], v[6:9], off sc0 sc1
	v_pk_mul_f32 v[16:17], v[154:155], s[0:1] op_sel_hi:[1,0]
	v_pk_mul_f32 v[20:21], v[150:151], s[0:1] op_sel_hi:[1,0]
	v_pk_mul_f32 v[8:9], v[158:159], s[0:1] op_sel_hi:[1,0]
	v_pk_mul_f32 v[24:25], v[146:147], s[0:1] op_sel_hi:[1,0]
	v_cvt_pk_fp8_f32 v6, v8, v9
	v_pk_mul_f32 v[12:13], v[160:161], s[0:1] op_sel_hi:[1,0]
	v_cvt_pk_fp8_f32 v7, v16, v17
	v_cvt_pk_fp8_f32 v8, v20, v21
	v_cvt_pk_fp8_f32 v9, v24, v25
	v_pk_mul_f32 v[14:15], v[156:157], s[0:1] op_sel_hi:[1,0]
	v_pk_mul_f32 v[18:19], v[152:153], s[0:1] op_sel_hi:[1,0]
	v_pk_mul_f32 v[22:23], v[148:149], s[0:1] op_sel_hi:[1,0]
	v_or_b32_e32 v10, 32, v4
	v_mov_b32_e32 v11, v5
	v_cvt_pk_fp8_f32 v6, v12, v13 op_sel:[0,0,1]
	v_cvt_pk_fp8_f32 v7, v14, v15 op_sel:[0,0,1]
	v_cvt_pk_fp8_f32 v8, v18, v19 op_sel:[0,0,1]
	v_cvt_pk_fp8_f32 v9, v22, v23 op_sel:[0,0,1]
	v_lshlrev_b64 v[10:11], 11, v[10:11]
	v_lshl_add_u64 v[10:11], s[6:7], 0, v[10:11]
	v_lshl_add_u64 v[10:11], v[10:11], 0, v[2:3]
	global_store_dwordx4 v[10:11], v[6:9], off sc0 sc1
	v_pk_mul_f32 v[16:17], v[138:139], s[0:1] op_sel_hi:[1,0]
	v_pk_mul_f32 v[20:21], v[134:135], s[0:1] op_sel_hi:[1,0]
	v_pk_mul_f32 v[8:9], v[142:143], s[0:1] op_sel_hi:[1,0]
	v_pk_mul_f32 v[24:25], v[130:131], s[0:1] op_sel_hi:[1,0]
	v_cvt_pk_fp8_f32 v6, v8, v9
	v_pk_mul_f32 v[12:13], v[144:145], s[0:1] op_sel_hi:[1,0]
	v_cvt_pk_fp8_f32 v7, v16, v17
	v_cvt_pk_fp8_f32 v8, v20, v21
	v_cvt_pk_fp8_f32 v9, v24, v25
	v_pk_mul_f32 v[14:15], v[140:141], s[0:1] op_sel_hi:[1,0]
	v_pk_mul_f32 v[18:19], v[136:137], s[0:1] op_sel_hi:[1,0]
	v_pk_mul_f32 v[22:23], v[132:133], s[0:1] op_sel_hi:[1,0]
	v_or_b32_e32 v10, 48, v4
	v_mov_b32_e32 v11, v5
	v_cvt_pk_fp8_f32 v6, v12, v13 op_sel:[0,0,1]
	v_cvt_pk_fp8_f32 v7, v14, v15 op_sel:[0,0,1]
	v_cvt_pk_fp8_f32 v8, v18, v19 op_sel:[0,0,1]
	v_cvt_pk_fp8_f32 v9, v22, v23 op_sel:[0,0,1]
	v_lshlrev_b64 v[10:11], 11, v[10:11]
	v_lshl_add_u64 v[10:11], s[6:7], 0, v[10:11]
	v_lshl_add_u64 v[10:11], v[10:11], 0, v[2:3]
	global_store_dwordx4 v[10:11], v[6:9], off sc0 sc1
	v_pk_mul_f32 v[16:17], v[122:123], s[0:1] op_sel_hi:[1,0]
	v_pk_mul_f32 v[20:21], v[118:119], s[0:1] op_sel_hi:[1,0]
	v_pk_mul_f32 v[8:9], v[126:127], s[0:1] op_sel_hi:[1,0]
	v_pk_mul_f32 v[24:25], v[114:115], s[0:1] op_sel_hi:[1,0]
	v_cvt_pk_fp8_f32 v6, v8, v9
	v_pk_mul_f32 v[12:13], v[128:129], s[0:1] op_sel_hi:[1,0]
	v_cvt_pk_fp8_f32 v7, v16, v17
	v_cvt_pk_fp8_f32 v8, v20, v21
	v_cvt_pk_fp8_f32 v9, v24, v25
	v_pk_mul_f32 v[14:15], v[124:125], s[0:1] op_sel_hi:[1,0]
	v_pk_mul_f32 v[18:19], v[120:121], s[0:1] op_sel_hi:[1,0]
	v_pk_mul_f32 v[22:23], v[116:117], s[0:1] op_sel_hi:[1,0]
	v_add_u32_e32 v10, 0x80, v4
	v_mov_b32_e32 v11, v5
	v_cvt_pk_fp8_f32 v6, v12, v13 op_sel:[0,0,1]
	v_cvt_pk_fp8_f32 v7, v14, v15 op_sel:[0,0,1]
	v_cvt_pk_fp8_f32 v8, v18, v19 op_sel:[0,0,1]
	v_cvt_pk_fp8_f32 v9, v22, v23 op_sel:[0,0,1]
	v_lshlrev_b64 v[10:11], 11, v[10:11]
	v_lshl_add_u64 v[10:11], s[6:7], 0, v[10:11]
	v_lshl_add_u64 v[10:11], v[10:11], 0, v[2:3]
	global_store_dwordx4 v[10:11], v[6:9], off sc0 sc1
	v_pk_mul_f32 v[16:17], v[106:107], s[0:1] op_sel_hi:[1,0]
	v_pk_mul_f32 v[20:21], v[102:103], s[0:1] op_sel_hi:[1,0]
	v_pk_mul_f32 v[8:9], v[110:111], s[0:1] op_sel_hi:[1,0]
	v_pk_mul_f32 v[24:25], v[98:99], s[0:1] op_sel_hi:[1,0]
	v_cvt_pk_fp8_f32 v6, v8, v9
	v_pk_mul_f32 v[12:13], v[112:113], s[0:1] op_sel_hi:[1,0]
	v_cvt_pk_fp8_f32 v7, v16, v17
	v_cvt_pk_fp8_f32 v8, v20, v21
	v_cvt_pk_fp8_f32 v9, v24, v25
	v_pk_mul_f32 v[14:15], v[108:109], s[0:1] op_sel_hi:[1,0]
	v_pk_mul_f32 v[18:19], v[104:105], s[0:1] op_sel_hi:[1,0]
	v_pk_mul_f32 v[22:23], v[100:101], s[0:1] op_sel_hi:[1,0]
	v_add_u32_e32 v10, 0x90, v4
	v_mov_b32_e32 v11, v5
	v_cvt_pk_fp8_f32 v6, v12, v13 op_sel:[0,0,1]
	v_cvt_pk_fp8_f32 v7, v14, v15 op_sel:[0,0,1]
	v_cvt_pk_fp8_f32 v8, v18, v19 op_sel:[0,0,1]
	v_cvt_pk_fp8_f32 v9, v22, v23 op_sel:[0,0,1]
	v_lshlrev_b64 v[10:11], 11, v[10:11]
	v_lshl_add_u64 v[10:11], s[6:7], 0, v[10:11]
	v_lshl_add_u64 v[10:11], v[10:11], 0, v[2:3]
	global_store_dwordx4 v[10:11], v[6:9], off sc0 sc1
	v_pk_mul_f32 v[16:17], v[90:91], s[0:1] op_sel_hi:[1,0]
	v_pk_mul_f32 v[20:21], v[86:87], s[0:1] op_sel_hi:[1,0]
	v_pk_mul_f32 v[8:9], v[94:95], s[0:1] op_sel_hi:[1,0]
	v_pk_mul_f32 v[24:25], v[82:83], s[0:1] op_sel_hi:[1,0]
	v_cvt_pk_fp8_f32 v6, v8, v9
	v_pk_mul_f32 v[12:13], v[96:97], s[0:1] op_sel_hi:[1,0]
	v_cvt_pk_fp8_f32 v7, v16, v17
	v_cvt_pk_fp8_f32 v8, v20, v21
	v_cvt_pk_fp8_f32 v9, v24, v25
	v_pk_mul_f32 v[14:15], v[92:93], s[0:1] op_sel_hi:[1,0]
	v_pk_mul_f32 v[18:19], v[88:89], s[0:1] op_sel_hi:[1,0]
	v_pk_mul_f32 v[22:23], v[84:85], s[0:1] op_sel_hi:[1,0]
	v_add_u32_e32 v10, 0xa0, v4
	v_mov_b32_e32 v11, v5
	v_cvt_pk_fp8_f32 v6, v12, v13 op_sel:[0,0,1]
	v_cvt_pk_fp8_f32 v7, v14, v15 op_sel:[0,0,1]
	v_cvt_pk_fp8_f32 v8, v18, v19 op_sel:[0,0,1]
	v_cvt_pk_fp8_f32 v9, v22, v23 op_sel:[0,0,1]
	v_lshlrev_b64 v[10:11], 11, v[10:11]
	v_lshl_add_u64 v[10:11], s[6:7], 0, v[10:11]
	v_lshl_add_u64 v[10:11], v[10:11], 0, v[2:3]
	global_store_dwordx4 v[10:11], v[6:9], off sc0 sc1
	v_pk_mul_f32 v[14:15], v[74:75], s[0:1] op_sel_hi:[1,0]
	v_pk_mul_f32 v[18:19], v[70:71], s[0:1] op_sel_hi:[1,0]
	v_pk_mul_f32 v[8:9], v[78:79], s[0:1] op_sel_hi:[1,0]
	v_pk_mul_f32 v[22:23], v[66:67], s[0:1] op_sel_hi:[1,0]
	v_cvt_pk_fp8_f32 v6, v8, v9
	v_pk_mul_f32 v[10:11], v[80:81], s[0:1] op_sel_hi:[1,0]
	v_cvt_pk_fp8_f32 v7, v14, v15
	v_cvt_pk_fp8_f32 v8, v18, v19
	v_cvt_pk_fp8_f32 v9, v22, v23
	v_pk_mul_f32 v[12:13], v[76:77], s[0:1] op_sel_hi:[1,0]
	v_pk_mul_f32 v[16:17], v[72:73], s[0:1] op_sel_hi:[1,0]
	v_pk_mul_f32 v[20:21], v[68:69], s[0:1] op_sel_hi:[1,0]
	v_add_u32_e32 v4, 0xb0, v4
	v_cvt_pk_fp8_f32 v6, v10, v11 op_sel:[0,0,1]
	v_cvt_pk_fp8_f32 v7, v12, v13 op_sel:[0,0,1]
	v_cvt_pk_fp8_f32 v8, v16, v17 op_sel:[0,0,1]
	v_cvt_pk_fp8_f32 v9, v20, v21 op_sel:[0,0,1]
	v_lshlrev_b64 v[4:5], 11, v[4:5]
	v_lshl_add_u64 v[4:5], s[6:7], 0, v[4:5]
	v_lshl_add_u64 v[2:3], v[4:5], 0, v[2:3]
	global_store_dwordx4 v[2:3], v[6:9], off sc0 sc1
	s_waitcnt vmcnt(0)
	s_cmpk_gt_u32 s3, 0xff
	s_cbranch_scc1 .LBB3_27
	s_barrier

.LBB4_30:
	s_lshl_b32 s0, s33, 8
	s_add_i32 s0, s0, 0
	v_lshl_add_u32 v0, v197, 6, s0
	v_lshl_or_b32 v1, s27, 6, v196
	v_add_u32_e32 v0, 0x20000, v0
	s_nop 15
	s_nop 15
	v_add_u32_e32 v22, s6, v1
	ds_read_b128 v[12:15], v0
	ds_read_b128 v[8:11], v0 offset:16
	ds_read_b128 v[4:7], v0 offset:32
	ds_read_b128 v[0:3], v0 offset:48
	s_waitcnt lgkmcnt(3)
	v_pk_mul_f32 v[20:21], v[188:189], v[12:13]
	s_waitcnt lgkmcnt(2)
	v_pk_mul_f32 v[28:29], v[184:185], v[8:9]
	s_waitcnt lgkmcnt(1)
	v_pk_mul_f32 v[32:33], v[180:181], v[4:5]
	s_waitcnt lgkmcnt(0)
	v_pk_mul_f32 v[36:37], v[176:177], v[0:1]
	v_cvt_pk_fp8_f32 v18, v20, v21
	v_lshlrev_b32_e32 v16, 4, v197
	v_cvt_pk_fp8_f32 v19, v28, v29
	v_cvt_pk_fp8_f32 v20, v32, v33
	v_cvt_pk_fp8_f32 v21, v36, v37
	v_lshl_or_b32 v16, s33, 6, v16
	v_or_b32_e32 v24, s2, v16
	v_pk_mul_f32 v[16:17], v[190:191], v[14:15]
	v_pk_mul_f32 v[26:27], v[186:187], v[10:11]
	v_pk_mul_f32 v[30:31], v[182:183], v[6:7]
	v_pk_mul_f32 v[34:35], v[178:179], v[2:3]
	v_ashrrev_i32_e32 v23, 31, v22
	v_cvt_pk_fp8_f32 v18, v16, v17 op_sel:[0,0,1]
	v_cvt_pk_fp8_f32 v19, v26, v27 op_sel:[0,0,1]
	v_cvt_pk_fp8_f32 v20, v30, v31 op_sel:[0,0,1]
	v_cvt_pk_fp8_f32 v21, v34, v35 op_sel:[0,0,1]
	v_lshlrev_b64 v[16:17], 13, v[22:23]
	v_ashrrev_i32_e32 v25, 31, v24
	v_lshl_add_u64 v[16:17], s[4:5], 0, v[16:17]
	v_lshl_add_u64 v[16:17], v[16:17], 0, v[24:25]
	global_store_dwordx4 v[16:17], v[18:21], off sc0 sc1
	v_pk_mul_f32 v[32:33], v[168:169], v[8:9]
	v_pk_mul_f32 v[36:37], v[164:165], v[4:5]
	v_pk_mul_f32 v[20:21], v[172:173], v[12:13]
	v_pk_mul_f32 v[40:41], v[160:161], v[0:1]
	v_cvt_pk_fp8_f32 v18, v20, v21
	v_or_b32_e32 v26, 16, v22
	v_cvt_pk_fp8_f32 v19, v32, v33
	v_cvt_pk_fp8_f32 v20, v36, v37
	v_cvt_pk_fp8_f32 v21, v40, v41
	v_pk_mul_f32 v[28:29], v[174:175], v[14:15]
	v_pk_mul_f32 v[30:31], v[170:171], v[10:11]
	v_pk_mul_f32 v[34:35], v[166:167], v[6:7]
	v_pk_mul_f32 v[38:39], v[162:163], v[2:3]
	v_ashrrev_i32_e32 v27, 31, v26
	v_cvt_pk_fp8_f32 v18, v28, v29 op_sel:[0,0,1]
	v_cvt_pk_fp8_f32 v19, v30, v31 op_sel:[0,0,1]
	v_cvt_pk_fp8_f32 v20, v34, v35 op_sel:[0,0,1]
	v_cvt_pk_fp8_f32 v21, v38, v39 op_sel:[0,0,1]
	v_lshlrev_b64 v[26:27], 13, v[26:27]
	v_lshl_add_u64 v[26:27], s[4:5], 0, v[26:27]
	v_lshl_add_u64 v[26:27], v[26:27], 0, v[24:25]
	global_store_dwordx4 v[26:27], v[18:21], off sc0 sc1
	v_pk_mul_f32 v[32:33], v[152:153], v[8:9]
	v_pk_mul_f32 v[36:37], v[148:149], v[4:5]
	v_pk_mul_f32 v[20:21], v[156:157], v[12:13]
	v_pk_mul_f32 v[40:41], v[144:145], v[0:1]
	v_cvt_pk_fp8_f32 v18, v20, v21
	v_or_b32_e32 v26, 32, v22
	v_cvt_pk_fp8_f32 v19, v32, v33
	v_cvt_pk_fp8_f32 v20, v36, v37
	v_cvt_pk_fp8_f32 v21, v40, v41
	v_pk_mul_f32 v[28:29], v[158:159], v[14:15]
	v_pk_mul_f32 v[30:31], v[154:155], v[10:11]
	v_pk_mul_f32 v[34:35], v[150:151], v[6:7]
	v_pk_mul_f32 v[38:39], v[146:147], v[2:3]
	v_ashrrev_i32_e32 v27, 31, v26
	v_cvt_pk_fp8_f32 v18, v28, v29 op_sel:[0,0,1]
	v_cvt_pk_fp8_f32 v19, v30, v31 op_sel:[0,0,1]
	v_cvt_pk_fp8_f32 v20, v34, v35 op_sel:[0,0,1]
	v_cvt_pk_fp8_f32 v21, v38, v39 op_sel:[0,0,1]
	v_lshlrev_b64 v[26:27], 13, v[26:27]
	v_lshl_add_u64 v[26:27], s[4:5], 0, v[26:27]
	v_lshl_add_u64 v[26:27], v[26:27], 0, v[24:25]
	global_store_dwordx4 v[26:27], v[18:21], off sc0 sc1
	v_pk_mul_f32 v[30:31], v[136:137], v[8:9]
	v_pk_mul_f32 v[34:35], v[132:133], v[4:5]
	v_pk_mul_f32 v[20:21], v[140:141], v[12:13]
	v_pk_mul_f32 v[38:39], v[128:129], v[0:1]
	v_cvt_pk_fp8_f32 v18, v20, v21
	v_or_b32_e32 v22, 48, v22
	v_cvt_pk_fp8_f32 v19, v30, v31
	v_cvt_pk_fp8_f32 v20, v34, v35
	v_cvt_pk_fp8_f32 v21, v38, v39
	v_pk_mul_f32 v[26:27], v[142:143], v[14:15]
	v_pk_mul_f32 v[28:29], v[138:139], v[10:11]
	v_pk_mul_f32 v[32:33], v[134:135], v[6:7]
	v_pk_mul_f32 v[36:37], v[130:131], v[2:3]
	v_ashrrev_i32_e32 v23, 31, v22
	v_cvt_pk_fp8_f32 v18, v26, v27 op_sel:[0,0,1]
	v_cvt_pk_fp8_f32 v19, v28, v29 op_sel:[0,0,1]
	v_cvt_pk_fp8_f32 v20, v32, v33 op_sel:[0,0,1]
	v_cvt_pk_fp8_f32 v21, v36, v37 op_sel:[0,0,1]
	v_lshlrev_b64 v[22:23], 13, v[22:23]
	v_lshl_add_u64 v[22:23], s[4:5], 0, v[22:23]
	v_lshl_add_u64 v[22:23], v[22:23], 0, v[24:25]
	global_store_dwordx4 v[22:23], v[18:21], off sc0 sc1
	v_pk_mul_f32 v[26:27], v[120:121], v[8:9]
	v_pk_mul_f32 v[30:31], v[116:117], v[4:5]
	v_pk_mul_f32 v[20:21], v[124:125], v[12:13]
	v_pk_mul_f32 v[34:35], v[112:113], v[0:1]
	v_cvt_pk_fp8_f32 v18, v20, v21
	v_pk_mul_f32 v[22:23], v[126:127], v[14:15]
	v_cvt_pk_fp8_f32 v19, v26, v27
	v_cvt_pk_fp8_f32 v20, v30, v31
	v_cvt_pk_fp8_f32 v21, v34, v35
	v_pk_mul_f32 v[24:25], v[122:123], v[10:11]
	v_pk_mul_f32 v[28:29], v[118:119], v[6:7]
	v_pk_mul_f32 v[32:33], v[114:115], v[2:3]
	v_cvt_pk_fp8_f32 v18, v22, v23 op_sel:[0,0,1]
	v_cvt_pk_fp8_f32 v19, v24, v25 op_sel:[0,0,1]
	v_cvt_pk_fp8_f32 v20, v28, v29 op_sel:[0,0,1]
	v_cvt_pk_fp8_f32 v21, v32, v33 op_sel:[0,0,1]
	s_mov_b32 s0, 0x100000
	v_add_co_u32_e32 v22, vcc, s0, v16
	v_pk_mul_f32 v[26:27], v[104:105], v[8:9]
	s_nop 0
	v_addc_co_u32_e32 v23, vcc, 0, v17, vcc
	global_store_dwordx4 v[22:23], v[18:21], off sc0 sc1
	v_pk_mul_f32 v[30:31], v[100:101], v[4:5]
	v_pk_mul_f32 v[34:35], v[96:97], v[0:1]
	v_pk_mul_f32 v[20:21], v[108:109], v[12:13]
	v_pk_mul_f32 v[22:23], v[110:111], v[14:15]
	v_cvt_pk_fp8_f32 v18, v20, v21
	v_cvt_pk_fp8_f32 v19, v26, v27
	v_cvt_pk_fp8_f32 v20, v30, v31
	v_cvt_pk_fp8_f32 v21, v34, v35
	v_pk_mul_f32 v[24:25], v[106:107], v[10:11]
	v_pk_mul_f32 v[28:29], v[102:103], v[6:7]
	v_pk_mul_f32 v[32:33], v[98:99], v[2:3]
	v_cvt_pk_fp8_f32 v18, v22, v23 op_sel:[0,0,1]
	v_cvt_pk_fp8_f32 v19, v24, v25 op_sel:[0,0,1]
	v_cvt_pk_fp8_f32 v20, v28, v29 op_sel:[0,0,1]
	v_cvt_pk_fp8_f32 v21, v32, v33 op_sel:[0,0,1]
	s_mov_b32 s0, 0x120000
	v_add_co_u32_e32 v22, vcc, s0, v16
	v_pk_mul_f32 v[26:27], v[88:89], v[8:9]
	s_nop 0
	v_addc_co_u32_e32 v23, vcc, 0, v17, vcc
	global_store_dwordx4 v[22:23], v[18:21], off sc0 sc1
	v_pk_mul_f32 v[30:31], v[84:85], v[4:5]
	v_pk_mul_f32 v[34:35], v[80:81], v[0:1]
	v_pk_mul_f32 v[20:21], v[92:93], v[12:13]
	v_pk_mul_f32 v[22:23], v[94:95], v[14:15]
	v_cvt_pk_fp8_f32 v18, v20, v21
	v_cvt_pk_fp8_f32 v19, v26, v27
	v_cvt_pk_fp8_f32 v20, v30, v31
	v_cvt_pk_fp8_f32 v21, v34, v35
	v_pk_mul_f32 v[24:25], v[90:91], v[10:11]
	v_pk_mul_f32 v[28:29], v[86:87], v[6:7]
	v_pk_mul_f32 v[32:33], v[82:83], v[2:3]
	v_cvt_pk_fp8_f32 v18, v22, v23 op_sel:[0,0,1]
	v_cvt_pk_fp8_f32 v19, v24, v25 op_sel:[0,0,1]
	v_cvt_pk_fp8_f32 v20, v28, v29 op_sel:[0,0,1]
	v_cvt_pk_fp8_f32 v21, v32, v33 op_sel:[0,0,1]
	s_mov_b32 s0, 0x140000
	v_add_co_u32_e32 v22, vcc, s0, v16
	v_pk_mul_f32 v[12:13], v[76:77], v[12:13]
	s_nop 0
	v_addc_co_u32_e32 v23, vcc, 0, v17, vcc
	global_store_dwordx4 v[22:23], v[18:21], off sc0 sc1
	v_pk_mul_f32 v[8:9], v[72:73], v[8:9]
	v_pk_mul_f32 v[4:5], v[68:69], v[4:5]
	v_pk_mul_f32 v[18:19], v[66:67], v[2:3]
	v_pk_mul_f32 v[20:21], v[64:65], v[0:1]
	v_pk_mul_f32 v[14:15], v[78:79], v[14:15]
	v_cvt_pk_fp8_f32 v0, v12, v13
	v_cvt_pk_fp8_f32 v1, v8, v9
	v_cvt_pk_fp8_f32 v2, v4, v5
	v_cvt_pk_fp8_f32 v3, v20, v21
	v_pk_mul_f32 v[10:11], v[74:75], v[10:11]
	v_pk_mul_f32 v[6:7], v[70:71], v[6:7]
	v_cvt_pk_fp8_f32 v0, v14, v15 op_sel:[0,0,1]
	v_cvt_pk_fp8_f32 v1, v10, v11 op_sel:[0,0,1]
	v_cvt_pk_fp8_f32 v2, v6, v7 op_sel:[0,0,1]
	v_cvt_pk_fp8_f32 v3, v18, v19 op_sel:[0,0,1]
	v_add_co_u32_e32 v4, vcc, 0x160000, v16
	s_cmpk_lt_u32 s26, 0x100
	s_nop 0
	v_addc_co_u32_e32 v5, vcc, 0, v17, vcc
	global_store_dwordx4 v[4:5], v[0:3], off sc0 sc1
	s_waitcnt vmcnt(0)
	s_cbranch_scc0 .LBB4_32
	s_barrier
